# baseline (speedup 1.0000x reference)
.LBB0_2:
	s_or_b64 exec, exec, s[6:7]
	v_bfe_u32 v16, v0, 6, 1
	v_lshl_or_b32 v2, v16, 4, v19
	s_movk_i32 s6, 0x80
	v_and_or_b32 v3, v0, s6, v18
	v_lshlrev_b32_e32 v6, 2, v2
	v_mad_u32_u24 v12, v2, s8, v3
	v_or_b32_e32 v2, 0x10a00, v6
	v_or_b32_e32 v6, 0x10a20, v6
	v_add_u32_e32 v14, 0x800, v12
	v_lshlrev_b32_e32 v50, 2, v0
	v_and_b32_e32 v50, 0x200, v50
	v_lshl_add_u32 v50, s2, 1, v50
	v_or_b32_e32 v50, v50, v16
	v_ashrrev_i32_e32 v51, 31, v50
	v_lshlrev_b64 v[50:51], 10, v[50:51]
	v_lshl_add_u64 v[50:51], s[12:13], 0, v[50:51]
	v_lshl_add_u64 v[50:51], v[50:51], 0, v[20:21]
	v_and_b32_e32 v40, 3, v0
	v_lshrrev_b32_e32 v41, 1, v40
	v_and_b32_e32 v42, 1, v40
	v_lshlrev_b32_e32 v41, 6, v41
	v_lshl_or_b32 v41, v42, 4, v41
	v_add_u32_e32 v44, 0x10a80, v41
	v_add_u32_e32 v45, 0x10a00, v41
	s_lshl_b32 s20, s2, 6
	v_lshl_add_u32 v46, v40, 4, s20
	v_cmp_gt_u32_e32 vcc, 4, v0
	s_waitcnt lgkmcnt(0)
	s_barrier
	ds_read2_b32 v[10:11], v12 offset1:68
	ds_read_b128 v[2:5], v2
	ds_read_b128 v[6:9], v6
	ds_read2_b32 v[52:53], v12 offset0:136 offset1:204
	ds_read2_b32 v[12:13], v14 offset0:32 offset1:100
	ds_read2_b32 v[14:15], v14 offset0:168 offset1:236
	ds_read_b128 v[54:57], v44
	ds_read_b128 v[58:61], v44 offset:32
	ds_read_b128 v[62:65], v45
	ds_read_b128 v[66:69], v45 offset:32
	s_waitcnt lgkmcnt(8)
	v_pk_mul_f32 v[2:3], v[10:11], v[2:3]
	s_waitcnt lgkmcnt(6)
	v_pk_mul_f32 v[4:5], v[52:53], v[4:5]
	v_cvt_pk_f16_f32 v2, v2, v3
	v_cvt_pk_f16_f32 v3, v4, v5
	s_waitcnt lgkmcnt(5)
	v_pk_mul_f32 v[4:5], v[12:13], v[6:7]
	s_waitcnt lgkmcnt(4)
	v_pk_mul_f32 v[6:7], v[14:15], v[8:9]
	v_cvt_pk_f16_f32 v4, v4, v5
	v_cvt_pk_f16_f32 v5, v6, v7
	global_store_dwordx4 v[50:51], v[2:5], off sc1
	s_and_saveexec_b64 s[4:5], vcc
	s_cbranch_execz .LBB0_4
	s_waitcnt lgkmcnt(0)
	v_cvt_pk_f16_f32 v54, v54, v55
	v_cvt_pk_f16_f32 v55, v56, v57
	v_cvt_pk_f16_f32 v56, v58, v59
	v_cvt_pk_f16_f32 v57, v60, v61
	v_cvt_pk_f16_f32 v62, v62, v63
	v_cvt_pk_f16_f32 v63, v64, v65
	v_cvt_pk_f16_f32 v64, v66, v67
	v_cvt_pk_f16_f32 v65, v68, v69
	global_store_dwordx4 v46, v[54:57], s[14:15] sc1
	global_store_dwordx4 v46, v[62:65], s[16:17] sc1
